# speedup vs baseline: 1.0013x; 1.0013x over previous
.LBB4_3:
	s_lshr_b32 s29, s35, 25
	s_add_i32 s29, s34, s29
	s_not_b32 s62, s30
	s_ashr_i32 s63, s29, 7
	s_add_i32 s64, s54, 0x18000
	v_and_b32_e32 v19, 15, v0
	v_and_b32_e32 v0, 4, v0
	s_add_u32 s30, s38, 0x80
	v_lshl_or_b32 v149, s15, 6, v19
	v_lshlrev_b32_e32 v20, 5, v1
	v_and_or_b32 v0, v18, 1, v0
	s_waitcnt vmcnt(0)
	s_barrier
	s_addc_u32 s31, s39, 0
	s_mov_b32 m0, s64
	s_nop 0
	global_load_lds_dwordx4 v148, s[30:31]
	s_add_i32 s65, s54, 0x1a000
	s_add_i32 s66, s54, 0x8000
	v_lshlrev_b32_e32 v21, 7, v149
	v_lshlrev_b32_e32 v0, 4, v0
	v_or_b32_e32 v23, 16, v20
	s_mov_b32 m0, s65
	s_nop 0
	global_load_lds_dwordx4 v152, s[30:31]
	s_add_u32 s30, s40, 0x80
	v_xor_b32_e32 v18, v0, v20
	v_bitop3_b32 v22, v21, v0, v20 bitop3:0xf6
	v_bitop3_b32 v20, v0, v20, 16 bitop3:0x1e
	v_bitop3_b32 v21, v21, v0, v23 bitop3:0xf6
	v_lshlrev_b32_e32 v0, 7, v19
	s_addc_u32 s31, s41, 0
	s_mov_b32 m0, s66
	s_nop 0
	global_load_lds_dwordx4 v146, s[30:31]
	s_add_i32 s67, s54, 0xa000
	s_add_i32 s68, s54, 0x1c000
	v_lshl_or_b32 v0, s4, 12, v0
	s_mov_b32 m0, s67
	s_nop 0
	global_load_lds_dwordx4 v150, s[30:31]
	s_add_u32 s0, s0, 0x80
	v_or3_b32 v18, v18, v0, s5
	v_or3_b32 v19, v20, v0, s5
	s_addc_u32 s1, s1, 0
	s_mov_b32 m0, s68
	s_nop 0
	global_load_lds_dwordx4 v148, s[0:1]
	v_lshlrev_b32_e32 v0, 4, v1
	s_add_i32 s69, s54, 0x1e000
	s_mov_b32 m0, s69
	s_nop 0
	global_load_lds_dwordx4 v152, s[0:1]
	v_and_b32_e32 v1, 32, v0
	v_and_b32_e32 v153, 16, v0
	v_or_b32_e32 v158, 32, v0
	v_div_scale_f32 v0, s[0:1], s13, s13, 1.0
	v_lshl_or_b32 v151, s4, 6, v1
	v_rcp_f32_e32 v1, v0
	s_cmpk_gt_i32 s34, 0x7f
	s_cselect_b64 s[30:31], -1, 0
	s_add_i32 s70, s54, 0xc000
	v_fma_f32 v20, -v0, v1, 1.0
	v_fmac_f32_e32 v1, v20, v1
	v_div_scale_f32 v20, vcc, 1.0, s13, 1.0
	v_mul_f32_e32 v23, v20, v1
	v_fma_f32 v24, -v0, v23, v20
	v_fmac_f32_e32 v23, v24, v1
	v_fma_f32 v0, -v0, v23, v20
	v_div_fmas_f32 v0, v0, v1, v23
	v_mov_b32_e32 v1, s14
	v_mul_f32_e32 v1, s13, v1
	v_div_scale_f32 v20, s[0:1], v1, v1, 1.0
	v_rcp_f32_e32 v23, v20
	s_add_i32 s71, s54, 0xe000
	s_ashr_i32 s72, s33, 31
	s_ashr_i32 s73, s2, 31
	v_fma_f32 v24, -v20, v23, 1.0
	v_fmac_f32_e32 v23, v24, v23
	v_div_scale_f32 v24, vcc, 1.0, v1, 1.0
	v_mul_f32_e32 v25, v24, v23
	v_fma_f32 v26, -v20, v25, v24
	v_fmac_f32_e32 v25, v26, v23
	v_fma_f32 v20, -v20, v25, v24
	s_waitcnt vmcnt(6)
	v_div_fmas_f32 v20, v20, v23, v25
	s_cmp_eq_u32 s63, 2
	v_div_fixup_f32 v0, v0, s13, 1.0
	v_div_fixup_f32 v159, v20, v1, 1.0
	s_cselect_b64 s[14:15], -1, 0
	s_cmpk_gt_u32 s34, 0x17f
	v_mov_b32_e32 v154, v0
	v_mov_b32_e32 v155, v0
	v_mul_f32_e32 v160, 0x40c00000, v159
	s_cselect_b64 s[34:35], -1, 0
	v_add_u32_e32 v161, 0, v18
	v_add_u32_e32 v162, 0, v19
	v_add_u32_e32 v163, 0, v22
	v_add_u32_e32 v164, 0, v21
	s_barrier
	s_branch .LBB4_5

.LBB5_3:
	s_lshr_b32 s29, s35, 25
	s_add_i32 s29, s34, s29
	s_not_b32 s63, s30
	s_ashr_i32 s64, s29, 7
	s_add_i32 s65, s55, 0x18000
	v_and_b32_e32 v19, 15, v0
	v_and_b32_e32 v0, 4, v0
	s_add_u32 s30, s40, 0x80
	v_lshl_or_b32 v149, s15, 6, v19
	v_lshlrev_b32_e32 v20, 5, v1
	v_and_or_b32 v0, v18, 1, v0
	s_waitcnt vmcnt(0)
	s_barrier
	s_addc_u32 s31, s41, 0
	s_mov_b32 m0, s65
	s_nop 0
	global_load_lds_dwordx4 v148, s[30:31]
	s_add_i32 s66, s55, 0x1a000
	s_add_i32 s67, s55, 0x8000
	v_lshlrev_b32_e32 v21, 7, v149
	v_lshlrev_b32_e32 v0, 4, v0
	v_or_b32_e32 v23, 16, v20
	s_mov_b32 m0, s66
	s_nop 0
	global_load_lds_dwordx4 v152, s[30:31]
	s_add_u32 s30, s42, 0x80
	v_xor_b32_e32 v18, v0, v20
	v_bitop3_b32 v22, v21, v0, v20 bitop3:0xf6
	v_bitop3_b32 v20, v0, v20, 16 bitop3:0x1e
	v_bitop3_b32 v21, v21, v0, v23 bitop3:0xf6
	v_lshlrev_b32_e32 v0, 7, v19
	s_addc_u32 s31, s43, 0
	s_mov_b32 m0, s67
	s_nop 0
	global_load_lds_dwordx4 v146, s[30:31]
	s_add_i32 s68, s55, 0xa000
	s_add_i32 s69, s55, 0x1c000
	v_lshl_or_b32 v0, s4, 12, v0
	s_mov_b32 m0, s68
	s_nop 0
	global_load_lds_dwordx4 v150, s[30:31]
	s_add_u32 s0, s0, 0x80
	v_or3_b32 v18, v18, v0, s5
	v_or3_b32 v19, v20, v0, s5
	s_addc_u32 s1, s1, 0
	s_mov_b32 m0, s69
	s_nop 0
	global_load_lds_dwordx4 v148, s[0:1]
	v_lshlrev_b32_e32 v0, 4, v1
	s_add_i32 s70, s55, 0x1e000
	s_mov_b32 m0, s70
	s_nop 0
	global_load_lds_dwordx4 v152, s[0:1]
	v_and_b32_e32 v1, 32, v0
	v_and_b32_e32 v153, 16, v0
	v_or_b32_e32 v160, 32, v0
	v_div_scale_f32 v0, s[0:1], s13, s13, 1.0
	v_lshl_or_b32 v151, s4, 6, v1
	v_rcp_f32_e32 v1, v0
	s_cmpk_gt_i32 s34, 0x7f
	s_cselect_b64 s[30:31], -1, 0
	s_add_i32 s71, s55, 0xc000
	v_fma_f32 v20, -v0, v1, 1.0
	v_fmac_f32_e32 v1, v20, v1
	v_div_scale_f32 v20, vcc, 1.0, s13, 1.0
	v_mul_f32_e32 v23, v20, v1
	v_fma_f32 v24, -v0, v23, v20
	v_fmac_f32_e32 v23, v24, v1
	v_fma_f32 v0, -v0, v23, v20
	v_div_fmas_f32 v0, v0, v1, v23
	v_mov_b32_e32 v1, s14
	v_mul_f32_e32 v1, s13, v1
	v_div_scale_f32 v20, s[0:1], v1, v1, 1.0
	v_rcp_f32_e32 v23, v20
	s_add_i32 s72, s55, 0xe000
	s_ashr_i32 s73, s33, 31
	s_ashr_i32 s74, s2, 31
	v_fma_f32 v24, -v20, v23, 1.0
	v_fmac_f32_e32 v23, v24, v23
	v_div_scale_f32 v24, vcc, 1.0, v1, 1.0
	v_mul_f32_e32 v25, v24, v23
	v_fma_f32 v26, -v20, v25, v24
	v_fmac_f32_e32 v25, v26, v23
	v_fma_f32 v20, -v20, v25, v24
	s_waitcnt vmcnt(6)
	v_div_fmas_f32 v20, v20, v23, v25
	s_cmp_eq_u32 s64, 2
	v_div_fixup_f32 v0, v0, s13, 1.0
	v_div_fixup_f32 v161, v20, v1, 1.0
	s_cselect_b64 s[14:15], -1, 0
	s_cmpk_gt_u32 s34, 0x17f
	v_mov_b32_e32 v154, v0
	v_mov_b32_e32 v155, v0
	v_mul_f32_e32 v162, 0x40c00000, v161
	s_cselect_b64 s[34:35], -1, 0
	s_mov_b32 s36, 0x3c23d70a
	v_add_u32_e32 v163, 0, v18
	v_add_u32_e32 v164, 0, v19
	v_add_u32_e32 v165, 0, v22
	v_add_u32_e32 v166, 0, v21
	s_barrier
	s_branch .LBB5_5

.LBB6_6:
	v_and_b32_e32 v20, 15, v0
	v_and_b32_e32 v0, 4, v0
	v_lshl_or_b32 v165, s38, 6, v20
	v_lshlrev_b32_e32 v21, 5, v1
	v_and_or_b32 v0, v19, 1, v0
	s_lshr_b32 s7, s7, 25
	v_lshlrev_b32_e32 v22, 7, v165
	v_lshlrev_b32_e32 v0, 4, v0
	v_or_b32_e32 v24, 16, v21
	s_add_i32 s7, s6, s7
	v_xor_b32_e32 v19, v0, v21
	v_bitop3_b32 v23, v22, v0, v21 bitop3:0xf6
	v_bitop3_b32 v21, v0, v21, 16 bitop3:0x1e
	v_bitop3_b32 v22, v22, v0, v24 bitop3:0xf6
	v_lshlrev_b32_e32 v0, 7, v20
	s_ashr_i32 s61, s7, 7
	v_lshl_or_b32 v0, s8, 12, v0
	s_add_i32 s62, s53, 0x18000
	v_or3_b32 v20, v19, v0, s26
	v_or3_b32 v21, v21, v0, s26
	s_add_u32 s26, s34, 0x80
	s_waitcnt vmcnt(0)
	s_barrier
	s_addc_u32 s27, s35, 0
	s_mov_b32 m0, s62
	s_nop 0
	global_load_lds_dwordx4 v164, s[26:27]
	s_add_i32 s63, s53, 0x1a000
	s_add_i32 s64, s53, 0x8000
	s_mov_b32 m0, s63
	s_nop 0
	global_load_lds_dwordx4 v168, s[26:27]
	s_add_u32 s26, s36, 0x80
	s_addc_u32 s27, s37, 0
	s_add_i32 s65, s53, 0xa000
	s_add_i32 s66, s53, 0x1c000
	s_add_u32 s0, s0, 0x80
	s_addc_u32 s1, s1, 0
	s_add_i32 s67, s53, 0x1e000
	s_mov_b32 m0, s64
	s_nop 0
	global_load_lds_dwordx4 v162, s[26:27]
	s_cmpk_gt_i32 s6, 0x7f
	s_mov_b32 m0, s65
	s_nop 0
	global_load_lds_dwordx4 v166, s[26:27]
	s_cselect_b64 s[26:27], -1, 0
	s_add_i32 s68, s53, 0xc000
	s_add_i32 s69, s53, 0xe000
	s_ashr_i32 s70, s51, 31
	s_ashr_i32 s71, s2, 31
	s_lshl_b32 s7, s8, 8
	s_add_u32 s28, s28, s7
	s_addc_u32 s29, s29, 0
	s_lshl_b32 s7, s8, 2
	s_mov_b32 m0, s66
	s_nop 0
	global_load_lds_dwordx4 v164, s[0:1]
	v_mov_b32_e32 v19, 0
	s_add_u32 s72, s12, s7
	s_mov_b32 m0, s67
	s_nop 0
	global_load_lds_dwordx4 v168, s[0:1]
	v_cmp_eq_u32_e64 s[0:1], 0, v1
	v_lshl_add_u64 v[0:1], s[28:29], 0, v[18:19]
	s_addc_u32 s73, s13, 0
	v_div_scale_f32 v18, s[12:13], s50, s50, 1.0
	v_rcp_f32_e32 v19, v18
	s_lshl_b32 s7, -1, s3
	s_not_b32 s74, s7
	s_add_i32 s7, s9, -1
	v_fma_f32 v24, -v18, v19, 1.0
	v_fmac_f32_e32 v19, v24, v19
	v_div_scale_f32 v24, vcc, 1.0, s50, 1.0
	v_mul_f32_e32 v25, v24, v19
	v_fma_f32 v26, -v18, v25, v24
	v_fmac_f32_e32 v25, v26, v19
	s_cmp_lg_u32 s11, 0
	v_fma_f32 v18, -v18, v25, v24
	s_waitcnt vmcnt(6)
	s_cselect_b32 s11, s7, -1
	v_div_fmas_f32 v18, v18, v19, v25
	s_cmp_eq_u32 s61, 2
	v_div_fixup_f32 v170, v18, s50, 1.0
	s_cselect_b64 s[12:13], -1, 0
	s_cmpk_gt_u32 s6, 0x17f
	v_mbcnt_lo_u32_b32 v18, -1, 0
	v_mov_b32_e32 v172, v170
	v_mov_b32_e32 v173, v170
	s_cselect_b64 s[28:29], -1, 0
	v_mov_b64_e32 v[174:175], s[4:5]
	v_mbcnt_hi_u32_b32 v167, -1, v18
	v_add_u32_e32 v169, 0, v20
	v_add_u32_e32 v178, 0, v21
	v_add_u32_e32 v179, 0, v23
	v_add_u32_e32 v180, 0, v22
	s_barrier
	s_branch .LBB6_8
